# speedup vs baseline: 1.0169x; 1.0169x over previous
.LBB2_22:
	ds_read_b128 v[170:173], v174
	ds_read_b128 v[180:183], v174 offset:2048
	ds_read_b128 v[202:205], v178
	ds_read_b128 v[206:209], v178 offset:2048
	s_mov_b32 s89, s65
	s_mov_b32 s65, s6
	ds_read_b128 v[162:165], v194
	ds_read_b128 v[150:153], v194 offset:2048
	ds_read_b128 v[166:169], v195
	ds_read_b128 v[154:157], v195 offset:2048
	ds_read_b128 v[146:149], v194 offset:4096
	ds_read_b128 v[138:141], v194 offset:6144
	ds_read_b128 v[158:161], v195 offset:4096
	ds_read_b128 v[142:145], v195 offset:6144
	s_waitcnt vmcnt(14)
	s_mul_i32 s94, s83, s35
	v_cvt_pk_f16_f32 v22, v22, v23
	v_cvt_pk_f16_f32 v23, v24, v25
	v_cvt_pk_f16_f32 v18, v18, v19
	v_cvt_pk_f16_f32 v19, v20, v21
	v_cvt_pk_f16_f32 v14, v14, v15
	v_cvt_pk_f16_f32 v15, v16, v17
	v_cvt_pk_f16_f32 v10, v10, v11
	v_cvt_pk_f16_f32 v11, v12, v13
	ds_write2st64_b64 v201, v[22:23], v[18:19] offset0:32 offset1:40
	ds_write2st64_b64 v201, v[14:15], v[10:11] offset0:48 offset1:56
	s_waitcnt vmcnt(12)
	s_lshl_b32 s6, s90, 6
	s_add_i32 s7, s94, s6
	s_lshl_b32 s7, s7, 2
	v_add_u32_e32 v210, s89, v193
	s_add_i32 s8, s7, s81
	s_mul_i32 s95, s84, s35
	ds_write_b128 v210, v[6:9] offset:32768
	ds_write_b128 v210, v[2:5] offset:40960
	s_add_i32 s9, s8, s81
	s_add_i32 s93, s95, s6
	s_add_i32 s10, s9, s81
	s_nop 4
	buffer_load_dwordx4 v[22:25], v192, s[56:59], s7 offen nt
	buffer_load_dwordx4 v[18:21], v192, s[56:59], s8 offen nt
	buffer_load_dwordx4 v[14:17], v192, s[56:59], s9 offen nt
	buffer_load_dwordx4 v[10:13], v192, s[56:59], s10 offen nt
	s_lshl_b32 s6, s93, 1
	s_add_i32 s7, s6, s81
	s_nop 4
	buffer_load_dwordx4 v[6:9], v191, s[48:51], s6 offen
	buffer_load_dwordx4 v[2:5], v191, s[48:51], s7 offen
	s_barrier
	s_waitcnt lgkmcnt(0)
	s_setprio 1
	s_waitcnt lgkmcnt(11)
	v_mfma_f32_16x16x32_f16 v[134:137], v[170:173], v[162:165], v[134:137]
	v_mfma_f32_16x16x32_f16 v[130:133], v[180:183], v[162:165], v[130:133]
	s_waitcnt lgkmcnt(10)
	v_mfma_f32_16x16x32_f16 v[126:129], v[170:173], v[150:153], v[126:129]
	v_mfma_f32_16x16x32_f16 v[122:125], v[180:183], v[150:153], v[122:125]
	s_waitcnt lgkmcnt(7)
	v_mfma_f32_16x16x32_f16 v[118:121], v[170:173], v[146:149], v[118:121]
	v_mfma_f32_16x16x32_f16 v[114:117], v[180:183], v[146:149], v[114:117]
	s_waitcnt lgkmcnt(6)
	v_mfma_f32_16x16x32_f16 v[110:113], v[170:173], v[138:141], v[110:113]
	v_mfma_f32_16x16x32_f16 v[106:109], v[180:183], v[138:141], v[106:109]
	v_mfma_f32_16x16x32_f16 v[134:137], v[202:205], v[166:169], v[134:137]
	v_mfma_f32_16x16x32_f16 v[130:133], v[206:209], v[166:169], v[130:133]
	v_mfma_f32_16x16x32_f16 v[126:129], v[202:205], v[154:157], v[126:129]
	v_mfma_f32_16x16x32_f16 v[122:125], v[206:209], v[154:157], v[122:125]
	s_waitcnt lgkmcnt(5)
	v_mfma_f32_16x16x32_f16 v[118:121], v[202:205], v[158:161], v[118:121]
	v_mfma_f32_16x16x32_f16 v[114:117], v[206:209], v[158:161], v[114:117]
	s_waitcnt lgkmcnt(4)
	v_mfma_f32_16x16x32_f16 v[110:113], v[202:205], v[142:145], v[110:113]
	v_mfma_f32_16x16x32_f16 v[106:109], v[206:209], v[142:145], v[106:109]
	s_setprio 0
	s_barrier
	ds_read_b128 v[170:173], v174 offset:16384
	ds_read_b128 v[174:177], v174 offset:18432
	ds_read_b128 v[182:185], v178 offset:16384
	ds_read_b128 v[178:181], v178 offset:18432
	s_waitcnt vmcnt(16)
	s_cmp_lt_u32 s92, 32
	ds_write_b128 v210, v[30:33] offset:49152
	ds_write_b128 v210, v[26:29] offset:57344
	s_waitcnt vmcnt(15)
	s_cbranch_scc0 .LBB2_28
	s_add_i32 s38, s64, s92
	s_lshl_b64 s[60:61], s[38:39], 3
	s_add_u32 s60, s60, s85
	v_cmp_ne_u32_e64 s[6:7], 0, v34
	v_cmp_ne_u32_e64 s[8:9], 0, v35
	v_cmp_ne_u32_e64 s[10:11], 0, v36
	v_cmp_ne_u32_e64 s[12:13], 0, v37
	s_addc_u32 s61, s61, 0
	s_nop 1
	s_and_b64 s[98:99], s[6:7], s[8:9]
	s_and_b64 s[100:101], s[10:11], s[12:13]
	s_and_b64 s[98:99], s[98:99], s[100:101]
	s_cmp_eq_u64 s[98:99], -1
	s_cbranch_scc0 .Lqkv_mslow_0
	s_lshl_b64 s[96:97], s[60:61], 5
	v_lshl_add_u64 v[26:27], v[0:1], 0, s[96:97]
	v_mov_b32_e32 v28, -1
	v_mov_b32_e32 v29, -1
	s_add_u32 s6, s42, s60
	s_addc_u32 s7, s43, s61
	s_mov_b64 exec, 15
	global_store_dwordx2 v[26:27], v[28:29], off
	s_mov_b64 exec, 1
	global_store_byte v187, v187, s[6:7]
	s_mov_b64 exec, -1
	s_branch .LBB2_28
.Lqkv_mslow_0:
	s_and_saveexec_b64 s[68:69], s[0:1]
	s_cbranch_execz .LBB2_25
	v_mov_b32_e32 v28, s13
	v_mov_b32_e32 v29, s11
	v_cndmask_b32_e64 v28, v28, v29, s[4:5]
	v_mov_b32_e32 v29, s12
	v_mov_b32_e32 v30, s10
	v_cndmask_b32_e64 v29, v29, v30, s[4:5]
	v_mov_b32_e32 v30, s8
	v_cndmask_b32_e64 v30, v29, v30, s[2:3]
	v_mov_b32_e32 v29, s9
	v_cndmask_b32_e64 v28, v28, v29, s[2:3]
	v_mov_b32_e32 v29, s7
	s_lshl_b64 s[96:97], s[60:61], 5
	v_cndmask_b32_e32 v29, v28, v29, vcc
	v_mov_b32_e32 v28, s6
	v_lshl_add_u64 v[26:27], v[0:1], 0, s[96:97]
	v_cndmask_b32_e32 v28, v30, v28, vcc
	global_store_dwordx2 v[26:27], v[28:29], off

.LBB2_28:
	s_add_i32 s93, s93, s81
	s_lshl_b32 s6, s93, 1
	s_add_i32 s91, s92, 2
	s_add_i32 s7, s6, s81
	s_add_i32 s8, s47, 0xffffe000
	s_cmp_lt_u32 s91, 32
	buffer_load_dwordx4 v[30:33], v191, s[48:51], s6 offen
	buffer_load_dwordx4 v[26:29], v191, s[48:51], s7 offen
	s_cselect_b64 s[6:7], -1, 0
	v_cndmask_b32_e64 v202, v200, v190, s[6:7]
	s_and_b64 s[6:7], s[6:7], exec
	s_cselect_b32 s6, s8, 0
	buffer_load_dwordx4 v[34:37], v202, s[52:55], s6 offen nt
	s_add_i32 s90, s90, 1
	s_cmp_lg_u32 s90, s82
	s_cbranch_scc1 .LBB2_32
	s_add_i32 s93, s86, 1
	s_cmp_gt_i32 s86, 1
	s_cbranch_scc1 .LBB2_31
	s_mul_i32 s6, s93, s33
	s_add_i32 s6, s6, s73
	s_abs_i32 s8, s6
	s_mul_hi_u32 s9, s8, s75
	s_mul_i32 s10, s9, s72
	s_ashr_i32 s7, s6, 31
	s_sub_i32 s8, s8, s10
	s_xor_b32 s7, s7, s74
	s_add_i32 s10, s9, 1
	s_sub_i32 s11, s8, s72
	s_cmp_ge_u32 s8, s72
	s_cselect_b32 s9, s10, s9
	s_cselect_b32 s8, s11, s8
	s_add_i32 s10, s9, 1
	s_cmp_ge_u32 s8, s72
	s_cselect_b32 s8, s10, s9
	s_xor_b32 s8, s8, s7
	s_sub_i32 s7, s8, s7
	s_mul_i32 s8, s7, s71
	s_sub_i32 s6, s6, s8
	s_abs_i32 s9, s6
	s_mul_hi_u32 s10, s9, s78
	s_mul_i32 s11, s10, s76
	s_ashr_i32 s8, s6, 31
	s_sub_i32 s9, s9, s11
	s_xor_b32 s8, s8, s77
	s_add_i32 s11, s10, 1
	s_sub_i32 s12, s9, s76
	s_cmp_ge_u32 s9, s76
	s_cselect_b32 s10, s11, s10
	s_cselect_b32 s9, s12, s9
	s_add_i32 s11, s10, 1
	s_cmp_ge_u32 s9, s76
	s_cselect_b32 s9, s11, s10
	s_xor_b32 s9, s9, s8
	s_sub_i32 s8, s9, s8
	s_lshl_b32 s83, s8, 7
	s_mul_i32 s8, s8, s70
	s_sub_i32 s6, s6, s8
	s_lshl_b32 s84, s6, 8
	s_cmp_eq_u32 s7, 1
	s_cselect_b32 s6, s19, s21
	s_cselect_b32 s8, s18, s20
	s_cselect_b32 s9, s25, s27
	s_cselect_b32 s10, s24, s26
	s_cmp_eq_u32 s7, 0
	s_cselect_b32 s6, s17, s6
	s_cselect_b32 s7, s23, s9
	s_cselect_b32 s56, s16, s8
	s_cselect_b32 s48, s22, s10
	s_and_b32 s57, s6, 0xffff
	s_and_b32 s49, s7, 0xffff
	s_mov_b32 s51, s15
	s_mul_i32 s94, s83, s35
	s_mul_i32 s95, s84, s35
	s_mov_b64 s[58:59], s[14:15]

.LBB2_33:
	s_barrier
	s_waitcnt lgkmcnt(0)
	s_setprio 1
	s_waitcnt lgkmcnt(5)
	v_mfma_f32_16x16x32_f16 v[102:105], v[170:173], v[162:165], v[102:105]
	s_waitcnt lgkmcnt(4)
	v_mfma_f32_16x16x32_f16 v[98:101], v[174:177], v[162:165], v[98:101]
	v_mfma_f32_16x16x32_f16 v[94:97], v[170:173], v[150:153], v[94:97]
	v_mfma_f32_16x16x32_f16 v[90:93], v[174:177], v[150:153], v[90:93]
	v_mfma_f32_16x16x32_f16 v[86:89], v[170:173], v[146:149], v[86:89]
	v_mfma_f32_16x16x32_f16 v[82:85], v[174:177], v[146:149], v[82:85]
	v_mfma_f32_16x16x32_f16 v[78:81], v[170:173], v[138:141], v[78:81]
	v_mfma_f32_16x16x32_f16 v[74:77], v[174:177], v[138:141], v[74:77]
	s_waitcnt lgkmcnt(3)
	v_mfma_f32_16x16x32_f16 v[102:105], v[182:185], v[166:169], v[102:105]
	s_waitcnt lgkmcnt(2)
	v_mfma_f32_16x16x32_f16 v[98:101], v[178:181], v[166:169], v[98:101]
	v_mfma_f32_16x16x32_f16 v[94:97], v[182:185], v[154:157], v[94:97]
	v_mfma_f32_16x16x32_f16 v[90:93], v[178:181], v[154:157], v[90:93]
	v_mfma_f32_16x16x32_f16 v[86:89], v[182:185], v[158:161], v[86:89]
	v_mfma_f32_16x16x32_f16 v[82:85], v[178:181], v[158:161], v[82:85]
	v_mfma_f32_16x16x32_f16 v[78:81], v[182:185], v[142:145], v[78:81]
	v_mfma_f32_16x16x32_f16 v[74:77], v[178:181], v[142:145], v[74:77]
	s_setprio 0
	s_barrier
	v_add_u32_e32 v202, s89, v196
	v_add_u32_e32 v203, s89, v186
	ds_read_b128 v[170:173], v202 offset:32768
	ds_read_b128 v[174:177], v202 offset:34816
	ds_read_b128 v[178:181], v203 offset:32768
	ds_read_b128 v[182:185], v203 offset:34816
	ds_read_b128 v[162:165], v194 offset:16384
	ds_read_b128 v[150:153], v194 offset:18432
	ds_read_b128 v[166:169], v195 offset:16384
	ds_read_b128 v[154:157], v195 offset:18432
	ds_read_b128 v[146:149], v194 offset:20480
	ds_read_b128 v[138:141], v194 offset:22528
	ds_read_b128 v[158:161], v195 offset:20480
	ds_read_b128 v[142:145], v195 offset:22528
	s_waitcnt vmcnt(14)
	s_lshl_b32 s86, s90, 6
	v_cvt_pk_f16_f32 v58, v58, v59
	v_cvt_pk_f16_f32 v59, v60, v61
	v_cvt_pk_f16_f32 v54, v54, v55
	v_cvt_pk_f16_f32 v55, v56, v57
	v_cvt_pk_f16_f32 v50, v50, v51
	v_cvt_pk_f16_f32 v51, v52, v53
	v_cvt_pk_f16_f32 v46, v46, v47
	v_cvt_pk_f16_f32 v47, v48, v49
	ds_write2st64_b64 v201, v[58:59], v[54:55] offset1:8
	ds_write2st64_b64 v201, v[50:51], v[46:47] offset0:16 offset1:24
	s_waitcnt vmcnt(12)
	s_add_i32 s6, s94, s86
	s_lshl_b32 s6, s6, 2
	v_add_u32_e32 v204, s87, v193
	s_add_i32 s7, s6, s81
	ds_write_b128 v204, v[42:45] offset:32768
	ds_write_b128 v204, v[38:41] offset:40960
	s_add_i32 s8, s7, s81
	s_add_i32 s9, s8, s81
	s_nop 4
	buffer_load_dwordx4 v[58:61], v192, s[56:59], s6 offen nt
	buffer_load_dwordx4 v[54:57], v192, s[56:59], s7 offen nt
	buffer_load_dwordx4 v[50:53], v192, s[56:59], s8 offen nt
	buffer_load_dwordx4 v[46:49], v192, s[56:59], s9 offen nt
	s_add_i32 s6, s95, s86
	s_lshl_b32 s6, s6, 1
	s_add_i32 s7, s6, s81
	s_nop 4
	buffer_load_dwordx4 v[42:45], v191, s[48:51], s6 offen
	buffer_load_dwordx4 v[38:41], v191, s[48:51], s7 offen
	s_barrier
	s_waitcnt lgkmcnt(0)
	s_setprio 1
	s_waitcnt lgkmcnt(11)
	v_mfma_f32_16x16x32_f16 v[134:137], v[170:173], v[162:165], v[134:137]
	v_mfma_f32_16x16x32_f16 v[130:133], v[174:177], v[162:165], v[130:133]
	s_waitcnt lgkmcnt(10)
	v_mfma_f32_16x16x32_f16 v[126:129], v[170:173], v[150:153], v[126:129]
	v_mfma_f32_16x16x32_f16 v[122:125], v[174:177], v[150:153], v[122:125]
	s_waitcnt lgkmcnt(7)
	v_mfma_f32_16x16x32_f16 v[118:121], v[170:173], v[146:149], v[118:121]
	v_mfma_f32_16x16x32_f16 v[114:117], v[174:177], v[146:149], v[114:117]
	s_waitcnt lgkmcnt(6)
	v_mfma_f32_16x16x32_f16 v[110:113], v[170:173], v[138:141], v[110:113]
	v_mfma_f32_16x16x32_f16 v[106:109], v[174:177], v[138:141], v[106:109]
	v_mfma_f32_16x16x32_f16 v[134:137], v[178:181], v[166:169], v[134:137]
	v_mfma_f32_16x16x32_f16 v[130:133], v[182:185], v[166:169], v[130:133]
	v_mfma_f32_16x16x32_f16 v[126:129], v[178:181], v[154:157], v[126:129]
	v_mfma_f32_16x16x32_f16 v[122:125], v[182:185], v[154:157], v[122:125]
	s_waitcnt lgkmcnt(5)
	v_mfma_f32_16x16x32_f16 v[118:121], v[178:181], v[158:161], v[118:121]
	v_mfma_f32_16x16x32_f16 v[114:117], v[182:185], v[158:161], v[114:117]
	s_waitcnt lgkmcnt(4)
	v_mfma_f32_16x16x32_f16 v[110:113], v[178:181], v[142:145], v[110:113]
	v_mfma_f32_16x16x32_f16 v[106:109], v[182:185], v[142:145], v[106:109]
	s_setprio 0
	s_barrier
	ds_read_b128 v[170:173], v202 offset:49152
	ds_read_b128 v[174:177], v202 offset:51200
	ds_read_b128 v[182:185], v203 offset:49152
	ds_read_b128 v[178:181], v203 offset:51200
	s_waitcnt vmcnt(16)
	s_cmp_gt_u32 s92, 30
	ds_write_b128 v204, v[66:69] offset:49152
	ds_write_b128 v204, v[62:65] offset:57344
	s_waitcnt vmcnt(15)
	s_cbranch_scc1 .LBB2_39
	s_add_i32 s38, s64, s92
	s_add_i32 s38, s38, 1
	s_lshl_b64 s[60:61], s[38:39], 3
	s_add_u32 s60, s60, s85
	v_cmp_ne_u32_e64 s[6:7], 0, v70
	v_cmp_ne_u32_e64 s[8:9], 0, v71
	v_cmp_ne_u32_e64 s[10:11], 0, v72
	v_cmp_ne_u32_e64 s[12:13], 0, v73
	s_addc_u32 s61, s61, 0
	s_nop 1
	s_and_b64 s[98:99], s[6:7], s[8:9]
	s_and_b64 s[100:101], s[10:11], s[12:13]
	s_and_b64 s[98:99], s[98:99], s[100:101]
	s_cmp_eq_u64 s[98:99], -1
	s_cbranch_scc0 .Lqkv_mslow_1
	s_lshl_b64 s[94:95], s[60:61], 5
	v_lshl_add_u64 v[62:63], v[0:1], 0, s[94:95]
	v_mov_b32_e32 v64, -1
	v_mov_b32_e32 v65, -1
	s_add_u32 s6, s42, s60
	s_addc_u32 s7, s43, s61
	s_mov_b64 exec, 15
	global_store_dwordx2 v[62:63], v[64:65], off
	s_mov_b64 exec, 1
	global_store_byte v187, v187, s[6:7]
	s_mov_b64 exec, -1
	s_branch .LBB2_39
.Lqkv_mslow_1:
	s_and_saveexec_b64 s[68:69], s[0:1]
	s_cbranch_execz .LBB2_36
	v_mov_b32_e32 v64, s13
	v_mov_b32_e32 v65, s11
	v_cndmask_b32_e64 v64, v64, v65, s[4:5]
	v_mov_b32_e32 v65, s12
	v_mov_b32_e32 v66, s10
	v_cndmask_b32_e64 v65, v65, v66, s[4:5]
	v_mov_b32_e32 v66, s8
	v_cndmask_b32_e64 v66, v65, v66, s[2:3]
	v_mov_b32_e32 v65, s9
	v_cndmask_b32_e64 v64, v64, v65, s[2:3]
	v_mov_b32_e32 v65, s7
	s_lshl_b64 s[94:95], s[60:61], 5
	v_cndmask_b32_e32 v65, v64, v65, vcc
	v_mov_b32_e32 v64, s6
	v_lshl_add_u64 v[62:63], v[0:1], 0, s[94:95]
	v_cndmask_b32_e32 v64, v66, v64, vcc
	global_store_dwordx2 v[62:63], v[64:65], off

.LBB2_39:
	s_add_i32 s6, s84, 0x80
	s_mul_i32 s6, s6, s35
	s_add_i32 s6, s6, s86
	s_lshl_b32 s6, s6, 1
	s_add_i32 s7, s6, s81
	s_cmp_lt_u32 s91, 31
	buffer_load_dwordx4 v[66:69], v191, s[48:51], s6 offen
	buffer_load_dwordx4 v[62:65], v191, s[48:51], s7 offen
	s_cselect_b64 s[6:7], -1, 0
	v_cndmask_b32_e64 v202, v200, v190, s[6:7]
	s_and_b64 s[6:7], s[6:7], exec
	s_cselect_b32 s6, s47, 0
	buffer_load_dwordx4 v[70:73], v202, s[52:55], s6 offen nt
	s_add_i32 s90, s90, 1
	s_cmp_lg_u32 s90, s82
	s_cbranch_scc1 .LBB2_43
	s_add_i32 s86, s93, 1
	s_cmp_gt_i32 s93, 1
	s_cbranch_scc1 .LBB2_42
	s_mul_i32 s6, s86, s33
	s_add_i32 s6, s6, s73
	s_abs_i32 s8, s6
	s_mul_hi_u32 s9, s8, s75
	s_mul_i32 s10, s9, s72
	s_ashr_i32 s7, s6, 31
	s_sub_i32 s8, s8, s10
	s_xor_b32 s7, s7, s74
	s_add_i32 s10, s9, 1
	s_sub_i32 s11, s8, s72
	s_cmp_ge_u32 s8, s72
	s_cselect_b32 s9, s10, s9
	s_cselect_b32 s8, s11, s8
	s_add_i32 s10, s9, 1
	s_cmp_ge_u32 s8, s72
	s_cselect_b32 s8, s10, s9
	s_xor_b32 s8, s8, s7
	s_sub_i32 s7, s8, s7
	s_mul_i32 s8, s7, s71
	s_sub_i32 s6, s6, s8
	s_abs_i32 s9, s6
	s_mul_hi_u32 s10, s9, s78
	s_mul_i32 s11, s10, s76
	s_ashr_i32 s8, s6, 31
	s_sub_i32 s9, s9, s11
	s_xor_b32 s8, s8, s77
	s_add_i32 s11, s10, 1
	s_sub_i32 s12, s9, s76
	s_cmp_ge_u32 s9, s76
	s_cselect_b32 s10, s11, s10
	s_cselect_b32 s9, s12, s9
	s_add_i32 s11, s10, 1
	s_cmp_ge_u32 s9, s76
	s_cselect_b32 s9, s11, s10
	s_xor_b32 s9, s9, s8
	s_sub_i32 s8, s9, s8
	s_lshl_b32 s83, s8, 7
	s_mul_i32 s8, s8, s70
	s_sub_i32 s6, s6, s8
	s_lshl_b32 s84, s6, 8
	s_cmp_eq_u32 s7, 1
	s_cselect_b32 s6, s19, s21
	s_cselect_b32 s8, s18, s20
	s_cselect_b32 s9, s25, s27
	s_cselect_b32 s10, s24, s26
	s_cmp_eq_u32 s7, 0
	s_cselect_b32 s6, s17, s6
	s_cselect_b32 s7, s23, s9
	s_cselect_b32 s56, s16, s8
	s_cselect_b32 s48, s22, s10
	s_and_b32 s57, s6, 0xffff
	s_and_b32 s49, s7, 0xffff
	s_mov_b32 s51, s15
	s_mov_b64 s[58:59], s[14:15]

.LBB2_48:
	s_endpgm
	s_nop 0
	s_nop 0
	s_nop 0
	s_nop 0
	s_nop 0
	s_nop 0
	s_nop 0
	s_nop 0
	s_nop 0
	s_nop 0
	s_endpgm

	.amdhsa_kernel _ZN4gemm15gemm128r_kernelILb1ELi0ELi3ELb1EEEvNS_7Args128E
		.amdhsa_group_segment_fixed_size 131072
		.amdhsa_private_segment_fixed_size 0
		.amdhsa_kernarg_size 376
		.amdhsa_user_sgpr_count 2
		.amdhsa_user_sgpr_dispatch_ptr 0
		.amdhsa_user_sgpr_queue_ptr 0
		.amdhsa_user_sgpr_kernarg_segment_ptr 1
		.amdhsa_user_sgpr_dispatch_id 0
		.amdhsa_user_sgpr_kernarg_preload_length 0
		.amdhsa_user_sgpr_kernarg_preload_offset 0
		.amdhsa_user_sgpr_private_segment_size 0
		.amdhsa_uses_dynamic_stack 0
		.amdhsa_enable_private_segment 0
		.amdhsa_system_sgpr_workgroup_id_x 1
		.amdhsa_system_sgpr_workgroup_id_y 0
		.amdhsa_system_sgpr_workgroup_id_z 0
		.amdhsa_system_sgpr_workgroup_info 0
		.amdhsa_system_vgpr_workitem_id 0
		.amdhsa_next_free_vgpr 211
		.amdhsa_next_free_sgpr 102
		.amdhsa_accum_offset 212
		.amdhsa_reserve_vcc 1
		.amdhsa_float_round_mode_32 0
		.amdhsa_float_round_mode_16_64 0
		.amdhsa_float_denorm_mode_32 3
		.amdhsa_float_denorm_mode_16_64 3
		.amdhsa_dx10_clamp 1
		.amdhsa_ieee_mode 1
		.amdhsa_fp16_overflow 0
		.amdhsa_tg_split 0
		.amdhsa_exception_fp_ieee_invalid_op 0
		.amdhsa_exception_fp_denorm_src 0
		.amdhsa_exception_fp_ieee_div_zero 0
		.amdhsa_exception_fp_ieee_overflow 0
		.amdhsa_exception_fp_ieee_underflow 0
		.amdhsa_exception_fp_ieee_inexact 0
		.amdhsa_exception_int_div_zero 0
	.end_amdhsa_kernel

amdhsa.kernels:
  - .agpr_count:     0
    .args:
      - .offset:         0
        .size:           64
        .value_kind:     by_value
    .group_segment_fixed_size: 0
    .kernarg_segment_align: 8
    .kernarg_segment_size: 64
    .language:       OpenCL C
    .language_version:
      - 2
      - 0
    .max_flat_workgroup_size: 256
    .name:           _Z11prep_kernel8PrepArgs
    .private_segment_fixed_size: 0
    .sgpr_count:     22
    .sgpr_spill_count: 0
    .symbol:         _Z11prep_kernel8PrepArgs.kd
    .uniform_work_group_size: 1
    .uses_dynamic_stack: false
    .vgpr_count:     38
    .vgpr_spill_count: 0
    .wavefront_size: 64
  - .agpr_count:     0
    .args:
      - .address_space:  global
        .offset:         0
        .size:           8
        .value_kind:     global_buffer
      - .address_space:  global
        .offset:         8
        .size:           8
        .value_kind:     global_buffer
      - .address_space:  global
        .offset:         16
        .size:           8
        .value_kind:     global_buffer
      - .address_space:  global
        .offset:         24
        .size:           8
        .value_kind:     global_buffer
      - .address_space:  global
        .offset:         32
        .size:           8
        .value_kind:     global_buffer
      - .address_space:  global
        .offset:         40
        .size:           8
        .value_kind:     global_buffer
    .group_segment_fixed_size: 83968
    .kernarg_segment_align: 8
    .kernarg_segment_size: 48
    .language:       OpenCL C
    .language_version:
      - 2
      - 0
    .max_flat_workgroup_size: 512
    .name:           _ZN4attn11attn_kernelEPKDF16_S1_S1_PDF16_PKyPKh
    .private_segment_fixed_size: 0
    .sgpr_count:     48
    .sgpr_spill_count: 0
    .symbol:         _ZN4attn11attn_kernelEPKDF16_S1_S1_PDF16_PKyPKh.kd
    .uniform_work_group_size: 1
    .uses_dynamic_stack: false
    .vgpr_count:     224
    .vgpr_spill_count: 0
    .wavefront_size: 64
  - .agpr_count:     0
    .args:
      - .offset:         0
        .size:           120
        .value_kind:     by_value
      - .offset:         120
        .size:           4
        .value_kind:     hidden_block_count_x
      - .offset:         124
        .size:           4
        .value_kind:     hidden_block_count_y
      - .offset:         128
        .size:           4
        .value_kind:     hidden_block_count_z
      - .offset:         132
        .size:           2
        .value_kind:     hidden_group_size_x
      - .offset:         134
        .size:           2
        .value_kind:     hidden_group_size_y
      - .offset:         136
        .size:           2
        .value_kind:     hidden_group_size_z
      - .offset:         138
        .size:           2
        .value_kind:     hidden_remainder_x
      - .offset:         140
        .size:           2
        .value_kind:     hidden_remainder_y
      - .offset:         142
        .size:           2
        .value_kind:     hidden_remainder_z
      - .offset:         160
        .size:           8
        .value_kind:     hidden_global_offset_x
      - .offset:         168
        .size:           8
        .value_kind:     hidden_global_offset_y
      - .offset:         176
        .size:           8
        .value_kind:     hidden_global_offset_z
      - .offset:         184
        .size:           2
        .value_kind:     hidden_grid_dims
    .group_segment_fixed_size: 131072
    .kernarg_segment_align: 8
    .kernarg_segment_size: 376
    .language:       OpenCL C
    .language_version:
      - 2
      - 0
    .max_flat_workgroup_size: 512
    .name:           _ZN4gemm15gemm128r_kernelILb1ELi0ELi3ELb1EEEvNS_7Args128E
    .private_segment_fixed_size: 0
    .sgpr_count:     108
    .sgpr_spill_count: 0
    .symbol:         _ZN4gemm15gemm128r_kernelILb1ELi0ELi3ELb1EEEvNS_7Args128E.kd
    .uniform_work_group_size: 1
    .uses_dynamic_stack: false
    .vgpr_count:     211
    .vgpr_spill_count: 0
    .wavefront_size: 64
  - .agpr_count:     0
    .args:
      - .offset:         0
        .size:           120
        .value_kind:     by_value
      - .offset:         120
        .size:           4
        .value_kind:     hidden_block_count_x
      - .offset:         124
        .size:           4
        .value_kind:     hidden_block_count_y
      - .offset:         128
        .size:           4
        .value_kind:     hidden_block_count_z
      - .offset:         132
        .size:           2
        .value_kind:     hidden_group_size_x
      - .offset:         134
        .size:           2
        .value_kind:     hidden_group_size_y
      - .offset:         136
        .size:           2
        .value_kind:     hidden_group_size_z
      - .offset:         138
        .size:           2
        .value_kind:     hidden_remainder_x
      - .offset:         140
        .size:           2
        .value_kind:     hidden_remainder_y
      - .offset:         142
        .size:           2
        .value_kind:     hidden_remainder_z
      - .offset:         160
        .size:           8
        .value_kind:     hidden_global_offset_x
      - .offset:         168
        .size:           8
        .value_kind:     hidden_global_offset_y
      - .offset:         176
        .size:           8
        .value_kind:     hidden_global_offset_z
      - .offset:         184
        .size:           2
        .value_kind:     hidden_grid_dims
    .group_segment_fixed_size: 131072
    .kernarg_segment_align: 8
    .kernarg_segment_size: 376
    .language:       OpenCL C
    .language_version:
      - 2
      - 0
    .max_flat_workgroup_size: 512
    .name:           _ZN4gemm15gemm128r_kernelILb0ELi1ELi1ELb0EEEvNS_7Args128E
    .private_segment_fixed_size: 0
    .sgpr_count:     75
    .sgpr_spill_count: 0
    .symbol:         _ZN4gemm15gemm128r_kernelILb0ELi1ELi1ELb0EEEvNS_7Args128E.kd
    .uniform_work_group_size: 1
    .uses_dynamic_stack: false
    .vgpr_count:     178
    .vgpr_spill_count: 0
    .wavefront_size: 64
